# bundle9 + N1 loop (layer>0): row B loads issued before waiting on row A (one exposed round trip per iteration instead of two)
# baseline (speedup 1.0000x reference)
.LBB0_204:
	s_and_b64 vcc, exec, s[86:87]
	v_lshl_add_u64 v[90:91], s[42:43], 0, v[84:85]
	s_cbranch_vccz .LBB0_246
	v_add_co_u32_e32 v24, vcc, 0x40100000, v90
	s_add_i32 s14, s17, -3
	s_nop 0
	v_addc_co_u32_e32 v25, vcc, 0, v91, vcc
	global_load_dwordx2 v[26:27], v[24:25], off nt
	global_load_dwordx2 v[28:29], v[24:25], off offset:512 nt
	global_load_dwordx2 v[30:31], v[24:25], off offset:1024 nt
	s_add_i32 s15, s17, -2
	v_readlane_b32 s6, v97, s14
	v_readlane_b32 s12, v97, s15
	s_ashr_i32 s7, s6, 31
	s_ashr_i32 s13, s12, 31
	s_lshl_b64 s[6:7], s[6:7], 10
	s_lshl_b64 s[12:13], s[12:13], 10
	v_lshl_add_u64 v[32:33], v[82:83], 0, s[6:7]
	v_lshl_add_u64 v[34:35], v[82:83], 0, s[12:13]
	global_load_dwordx2 v[24:25], v[24:25], off offset:1536 nt
	s_nop 0
	global_load_dword v100, v[32:33], off nt
	global_load_dword v64, v[34:35], off nt
	global_load_dword v101, v[32:33], off offset:256 nt
	global_load_dword v98, v[34:35], off offset:256 nt
	global_load_dword v102, v[32:33], off offset:512 nt
	global_load_dword v99, v[34:35], off offset:512 nt
	global_load_dword v103, v[34:35], off offset:768 nt
	global_load_dword v104, v[32:33], off offset:768 nt
	v_readlane_b32 s6, v96, s14
	v_readlane_b32 s12, v96, s15
	s_mov_b32 s7, s9
	s_mov_b32 s13, s11
	v_add_co_u32_e32 v16, vcc, 0x40100000, v90
	s_add_i32 s14, s17, -1
	s_nop 0
	v_addc_co_u32_e32 v17, vcc, 0, v91, vcc
	global_load_dwordx2 v[18:19], v[16:17], off offset:2048 nt
	global_load_dwordx2 v[20:21], v[16:17], off offset:2560 nt
	global_load_dwordx2 v[118:119], v[16:17], off offset:3072 nt
	v_readlane_b32 s8, v97, s14
	v_readlane_b32 s10, v97, s17
	s_ashr_i32 s9, s8, 31
	s_ashr_i32 s11, s10, 31
	s_lshl_b64 s[8:9], s[8:9], 10
	s_lshl_b64 s[10:11], s[10:11], 10
	v_lshl_add_u64 v[22:23], v[82:83], 0, s[8:9]
	v_lshl_add_u64 v[122:123], v[82:83], 0, s[10:11]
	global_load_dwordx2 v[120:121], v[16:17], off offset:3584 nt
	global_load_dword v108, v[22:23], off nt
	global_load_dword v105, v[122:123], off nt
	global_load_dword v109, v[22:23], off offset:256 nt
	global_load_dword v106, v[122:123], off offset:256 nt
	global_load_dword v110, v[22:23], off offset:512 nt
	global_load_dword v107, v[122:123], off offset:512 nt
	global_load_dword v111, v[122:123], off offset:768 nt
	global_load_dword v112, v[22:23], off offset:768 nt
	v_readlane_b32 s11, v96, s17
	v_readlane_b32 s9, v96, s14
	s_mov_b32 s8, s6
	s_mov_b32 s10, s12
	s_waitcnt vmcnt(23)
	v_cvt_f32_f16_e32 v44, v26
	v_cvt_f32_f16_e32 v46, v27
	v_cvt_f32_f16_sdwa v47, v27 dst_sel:DWORD dst_unused:UNUSED_PAD src0_sel:WORD_1
	v_cvt_f32_f16_sdwa v45, v26 dst_sel:DWORD dst_unused:UNUSED_PAD src0_sel:WORD_1
	s_waitcnt vmcnt(22)
	v_cvt_f32_f16_e32 v40, v28
	v_cvt_f32_f16_e32 v42, v29
	v_cvt_f32_f16_sdwa v43, v29 dst_sel:DWORD dst_unused:UNUSED_PAD src0_sel:WORD_1
	v_cvt_f32_f16_sdwa v41, v28 dst_sel:DWORD dst_unused:UNUSED_PAD src0_sel:WORD_1
	s_waitcnt vmcnt(21)
	v_cvt_f32_f16_e32 v36, v30
	v_cvt_f32_f16_e32 v38, v31
	v_cvt_f32_f16_sdwa v39, v31 dst_sel:DWORD dst_unused:UNUSED_PAD src0_sel:WORD_1
	v_cvt_f32_f16_sdwa v37, v30 dst_sel:DWORD dst_unused:UNUSED_PAD src0_sel:WORD_1
	s_waitcnt vmcnt(20)
	v_cvt_f32_f16_e32 v32, v24
	v_cvt_f32_f16_e32 v34, v25
	v_cvt_f32_f16_sdwa v35, v25 dst_sel:DWORD dst_unused:UNUSED_PAD src0_sel:WORD_1
	v_cvt_f32_f16_sdwa v33, v24 dst_sel:DWORD dst_unused:UNUSED_PAD src0_sel:WORD_1
	s_waitcnt vmcnt(11)
	v_cvt_f32_f16_e32 v28, v18
	v_cvt_f32_f16_e32 v30, v19
	v_cvt_f32_f16_sdwa v31, v19 dst_sel:DWORD dst_unused:UNUSED_PAD src0_sel:WORD_1
	v_cvt_f32_f16_sdwa v29, v18 dst_sel:DWORD dst_unused:UNUSED_PAD src0_sel:WORD_1
	s_waitcnt vmcnt(10)
	v_cvt_f32_f16_e32 v24, v20
	v_cvt_f32_f16_e32 v26, v21
	v_cvt_f32_f16_sdwa v27, v21 dst_sel:DWORD dst_unused:UNUSED_PAD src0_sel:WORD_1
	v_cvt_f32_f16_sdwa v25, v20 dst_sel:DWORD dst_unused:UNUSED_PAD src0_sel:WORD_1
	s_waitcnt vmcnt(9)
	v_cvt_f32_f16_e32 v20, v118
	v_cvt_f32_f16_e32 v22, v119
	v_cvt_f32_f16_sdwa v23, v119 dst_sel:DWORD dst_unused:UNUSED_PAD src0_sel:WORD_1
	v_cvt_f32_f16_sdwa v21, v118 dst_sel:DWORD dst_unused:UNUSED_PAD src0_sel:WORD_1
	s_waitcnt vmcnt(8)
	v_cvt_f32_f16_e32 v16, v120
	v_cvt_f32_f16_e32 v18, v121
	v_cvt_f32_f16_sdwa v19, v121 dst_sel:DWORD dst_unused:UNUSED_PAD src0_sel:WORD_1
	v_cvt_f32_f16_sdwa v17, v120 dst_sel:DWORD dst_unused:UNUSED_PAD src0_sel:WORD_1
	s_branch .LBB0_210
